# k_csr: batched (4 at a time) LDS position atomics in the CSR scatter pass when the bucket segment fits LDS
# speedup vs baseline: 1.0155x; 1.0094x over previous
.LBB1_56:
	s_or_b64 exec, exec, s[74:75]
	s_waitcnt lgkmcnt(0)
	s_barrier
	s_and_b64 vcc, exec, s[72:73]
	s_cbranch_vccnz .Lcsr_slow
	s_mov_b64 s[74:75], exec
	v_mov_b32_e32 v63, 2
	v_mov_b32_e32 v64, 1
	s_mov_b64 exec, s[30:31]
	v_lshlrev_b32_sdwa v58, v63, v30 dst_sel:DWORD dst_unused:UNUSED_PAD src0_sel:DWORD src1_sel:BYTE_0
	s_nop 0
	ds_add_rtn_u32 v58, v58, v64 offset:17408
	s_mov_b64 exec, s[66:67]
	v_lshlrev_b32_sdwa v59, v63, v31 dst_sel:DWORD dst_unused:UNUSED_PAD src0_sel:DWORD src1_sel:BYTE_0
	s_nop 0
	ds_add_rtn_u32 v59, v59, v64 offset:17408
	s_mov_b64 exec, s[64:65]
	v_lshlrev_b32_sdwa v60, v63, v32 dst_sel:DWORD dst_unused:UNUSED_PAD src0_sel:DWORD src1_sel:BYTE_0
	s_nop 0
	ds_add_rtn_u32 v60, v60, v64 offset:17408
	s_mov_b64 exec, s[62:63]
	v_lshlrev_b32_sdwa v61, v63, v33 dst_sel:DWORD dst_unused:UNUSED_PAD src0_sel:DWORD src1_sel:BYTE_0
	s_nop 0
	ds_add_rtn_u32 v61, v61, v64 offset:17408
	s_waitcnt lgkmcnt(0)
	s_mov_b64 exec, s[30:31]
	v_lshlrev_b32_e32 v58, 1, v58
	v_lshrrev_b32_e32 v62, 8, v30
	ds_write_b16 v58, v62
	s_mov_b64 exec, s[66:67]
	v_lshlrev_b32_e32 v59, 1, v59
	v_lshrrev_b32_e32 v62, 8, v31
	ds_write_b16 v59, v62
	s_mov_b64 exec, s[64:65]
	v_lshlrev_b32_e32 v60, 1, v60
	v_lshrrev_b32_e32 v62, 8, v32
	ds_write_b16 v60, v62
	s_mov_b64 exec, s[62:63]
	v_lshlrev_b32_e32 v61, 1, v61
	v_lshrrev_b32_e32 v62, 8, v33
	ds_write_b16 v61, v62
	s_cmp_eq_u64 s[60:61], 0
	s_cbranch_scc1 .Lcsr_fast_done
	s_mov_b64 exec, s[60:61]
	v_lshlrev_b32_sdwa v58, v63, v26 dst_sel:DWORD dst_unused:UNUSED_PAD src0_sel:DWORD src1_sel:BYTE_0
	s_nop 0
	ds_add_rtn_u32 v58, v58, v64 offset:17408
	s_mov_b64 exec, s[58:59]
	v_lshlrev_b32_sdwa v59, v63, v27 dst_sel:DWORD dst_unused:UNUSED_PAD src0_sel:DWORD src1_sel:BYTE_0
	s_nop 0
	ds_add_rtn_u32 v59, v59, v64 offset:17408
	s_mov_b64 exec, s[56:57]
	v_lshlrev_b32_sdwa v60, v63, v28 dst_sel:DWORD dst_unused:UNUSED_PAD src0_sel:DWORD src1_sel:BYTE_0
	s_nop 0
	ds_add_rtn_u32 v60, v60, v64 offset:17408
	s_mov_b64 exec, s[54:55]
	v_lshlrev_b32_sdwa v61, v63, v29 dst_sel:DWORD dst_unused:UNUSED_PAD src0_sel:DWORD src1_sel:BYTE_0
	s_nop 0
	ds_add_rtn_u32 v61, v61, v64 offset:17408
	s_waitcnt lgkmcnt(0)
	s_mov_b64 exec, s[60:61]
	v_lshlrev_b32_e32 v58, 1, v58
	v_lshrrev_b32_e32 v62, 8, v26
	ds_write_b16 v58, v62
	s_mov_b64 exec, s[58:59]
	v_lshlrev_b32_e32 v59, 1, v59
	v_lshrrev_b32_e32 v62, 8, v27
	ds_write_b16 v59, v62
	s_mov_b64 exec, s[56:57]
	v_lshlrev_b32_e32 v60, 1, v60
	v_lshrrev_b32_e32 v62, 8, v28
	ds_write_b16 v60, v62
	s_mov_b64 exec, s[54:55]
	v_lshlrev_b32_e32 v61, 1, v61
	v_lshrrev_b32_e32 v62, 8, v29
	ds_write_b16 v61, v62
	s_cmp_eq_u64 s[52:53], 0
	s_cbranch_scc1 .Lcsr_fast_done
	s_mov_b64 exec, s[52:53]
	v_lshlrev_b32_sdwa v58, v63, v22 dst_sel:DWORD dst_unused:UNUSED_PAD src0_sel:DWORD src1_sel:BYTE_0
	s_nop 0
	ds_add_rtn_u32 v58, v58, v64 offset:17408
	s_mov_b64 exec, s[50:51]
	v_lshlrev_b32_sdwa v59, v63, v23 dst_sel:DWORD dst_unused:UNUSED_PAD src0_sel:DWORD src1_sel:BYTE_0
	s_nop 0
	ds_add_rtn_u32 v59, v59, v64 offset:17408
	s_mov_b64 exec, s[48:49]
	v_lshlrev_b32_sdwa v60, v63, v24 dst_sel:DWORD dst_unused:UNUSED_PAD src0_sel:DWORD src1_sel:BYTE_0
	s_nop 0
	ds_add_rtn_u32 v60, v60, v64 offset:17408
	s_mov_b64 exec, s[46:47]
	v_lshlrev_b32_sdwa v61, v63, v25 dst_sel:DWORD dst_unused:UNUSED_PAD src0_sel:DWORD src1_sel:BYTE_0
	s_nop 0
	ds_add_rtn_u32 v61, v61, v64 offset:17408
	s_waitcnt lgkmcnt(0)
	s_mov_b64 exec, s[52:53]
	v_lshlrev_b32_e32 v58, 1, v58
	v_lshrrev_b32_e32 v62, 8, v22
	ds_write_b16 v58, v62
	s_mov_b64 exec, s[50:51]
	v_lshlrev_b32_e32 v59, 1, v59
	v_lshrrev_b32_e32 v62, 8, v23
	ds_write_b16 v59, v62
	s_mov_b64 exec, s[48:49]
	v_lshlrev_b32_e32 v60, 1, v60
	v_lshrrev_b32_e32 v62, 8, v24
	ds_write_b16 v60, v62
	s_mov_b64 exec, s[46:47]
	v_lshlrev_b32_e32 v61, 1, v61
	v_lshrrev_b32_e32 v62, 8, v25
	ds_write_b16 v61, v62
	s_cmp_eq_u64 s[44:45], 0
	s_cbranch_scc1 .Lcsr_fast_done
	s_mov_b64 exec, s[44:45]
	v_lshlrev_b32_sdwa v58, v63, v18 dst_sel:DWORD dst_unused:UNUSED_PAD src0_sel:DWORD src1_sel:BYTE_0
	s_nop 0
	ds_add_rtn_u32 v58, v58, v64 offset:17408
	s_mov_b64 exec, s[42:43]
	v_lshlrev_b32_sdwa v59, v63, v19 dst_sel:DWORD dst_unused:UNUSED_PAD src0_sel:DWORD src1_sel:BYTE_0
	s_nop 0
	ds_add_rtn_u32 v59, v59, v64 offset:17408
	s_mov_b64 exec, s[40:41]
	v_lshlrev_b32_sdwa v60, v63, v20 dst_sel:DWORD dst_unused:UNUSED_PAD src0_sel:DWORD src1_sel:BYTE_0
	s_nop 0
	ds_add_rtn_u32 v60, v60, v64 offset:17408
	s_mov_b64 exec, s[38:39]
	v_lshlrev_b32_sdwa v61, v63, v21 dst_sel:DWORD dst_unused:UNUSED_PAD src0_sel:DWORD src1_sel:BYTE_0
	s_nop 0
	ds_add_rtn_u32 v61, v61, v64 offset:17408
	s_waitcnt lgkmcnt(0)
	s_mov_b64 exec, s[44:45]
	v_lshlrev_b32_e32 v58, 1, v58
	v_lshrrev_b32_e32 v62, 8, v18
	ds_write_b16 v58, v62
	s_mov_b64 exec, s[42:43]
	v_lshlrev_b32_e32 v59, 1, v59
	v_lshrrev_b32_e32 v62, 8, v19
	ds_write_b16 v59, v62
	s_mov_b64 exec, s[40:41]
	v_lshlrev_b32_e32 v60, 1, v60
	v_lshrrev_b32_e32 v62, 8, v20
	ds_write_b16 v60, v62
	s_mov_b64 exec, s[38:39]
	v_lshlrev_b32_e32 v61, 1, v61
	v_lshrrev_b32_e32 v62, 8, v21
	ds_write_b16 v61, v62
	s_cmp_eq_u64 s[36:37], 0
	s_cbranch_scc1 .Lcsr_fast_done
	s_mov_b64 exec, s[36:37]
	v_lshlrev_b32_sdwa v58, v63, v14 dst_sel:DWORD dst_unused:UNUSED_PAD src0_sel:DWORD src1_sel:BYTE_0
	s_nop 0
	ds_add_rtn_u32 v58, v58, v64 offset:17408
	s_mov_b64 exec, s[34:35]
	v_lshlrev_b32_sdwa v59, v63, v15 dst_sel:DWORD dst_unused:UNUSED_PAD src0_sel:DWORD src1_sel:BYTE_0
	s_nop 0
	ds_add_rtn_u32 v59, v59, v64 offset:17408
	s_mov_b64 exec, s[28:29]
	v_lshlrev_b32_sdwa v60, v63, v16 dst_sel:DWORD dst_unused:UNUSED_PAD src0_sel:DWORD src1_sel:BYTE_0
	s_nop 0
	ds_add_rtn_u32 v60, v60, v64 offset:17408
	s_mov_b64 exec, s[26:27]
	v_lshlrev_b32_sdwa v61, v63, v17 dst_sel:DWORD dst_unused:UNUSED_PAD src0_sel:DWORD src1_sel:BYTE_0
	s_nop 0
	ds_add_rtn_u32 v61, v61, v64 offset:17408
	s_waitcnt lgkmcnt(0)
	s_mov_b64 exec, s[36:37]
	v_lshlrev_b32_e32 v58, 1, v58
	v_lshrrev_b32_e32 v62, 8, v14
	ds_write_b16 v58, v62
	s_mov_b64 exec, s[34:35]
	v_lshlrev_b32_e32 v59, 1, v59
	v_lshrrev_b32_e32 v62, 8, v15
	ds_write_b16 v59, v62
	s_mov_b64 exec, s[28:29]
	v_lshlrev_b32_e32 v60, 1, v60
	v_lshrrev_b32_e32 v62, 8, v16
	ds_write_b16 v60, v62
	s_mov_b64 exec, s[26:27]
	v_lshlrev_b32_e32 v61, 1, v61
	v_lshrrev_b32_e32 v62, 8, v17
	ds_write_b16 v61, v62
	s_cmp_eq_u64 s[24:25], 0
	s_cbranch_scc1 .Lcsr_fast_done
	s_mov_b64 exec, s[24:25]
	v_lshlrev_b32_sdwa v58, v63, v10 dst_sel:DWORD dst_unused:UNUSED_PAD src0_sel:DWORD src1_sel:BYTE_0
	s_nop 0
	ds_add_rtn_u32 v58, v58, v64 offset:17408
	s_mov_b64 exec, s[22:23]
	v_lshlrev_b32_sdwa v59, v63, v11 dst_sel:DWORD dst_unused:UNUSED_PAD src0_sel:DWORD src1_sel:BYTE_0
	s_nop 0
	ds_add_rtn_u32 v59, v59, v64 offset:17408
	s_mov_b64 exec, s[20:21]
	v_lshlrev_b32_sdwa v60, v63, v12 dst_sel:DWORD dst_unused:UNUSED_PAD src0_sel:DWORD src1_sel:BYTE_0
	s_nop 0
	ds_add_rtn_u32 v60, v60, v64 offset:17408
	s_mov_b64 exec, s[18:19]
	v_lshlrev_b32_sdwa v61, v63, v13 dst_sel:DWORD dst_unused:UNUSED_PAD src0_sel:DWORD src1_sel:BYTE_0
	s_nop 0
	ds_add_rtn_u32 v61, v61, v64 offset:17408
	s_waitcnt lgkmcnt(0)
	s_mov_b64 exec, s[24:25]
	v_lshlrev_b32_e32 v58, 1, v58
	v_lshrrev_b32_e32 v62, 8, v10
	ds_write_b16 v58, v62
	s_mov_b64 exec, s[22:23]
	v_lshlrev_b32_e32 v59, 1, v59
	v_lshrrev_b32_e32 v62, 8, v11
	ds_write_b16 v59, v62
	s_mov_b64 exec, s[20:21]
	v_lshlrev_b32_e32 v60, 1, v60
	v_lshrrev_b32_e32 v62, 8, v12
	ds_write_b16 v60, v62
	s_mov_b64 exec, s[18:19]
	v_lshlrev_b32_e32 v61, 1, v61
	v_lshrrev_b32_e32 v62, 8, v13
	ds_write_b16 v61, v62
	s_cmp_eq_u64 s[16:17], 0
	s_cbranch_scc1 .Lcsr_fast_done
	s_mov_b64 exec, s[16:17]
	v_lshlrev_b32_sdwa v58, v63, v6 dst_sel:DWORD dst_unused:UNUSED_PAD src0_sel:DWORD src1_sel:BYTE_0
	s_nop 0
	ds_add_rtn_u32 v58, v58, v64 offset:17408
	s_mov_b64 exec, s[14:15]
	v_lshlrev_b32_sdwa v59, v63, v7 dst_sel:DWORD dst_unused:UNUSED_PAD src0_sel:DWORD src1_sel:BYTE_0
	s_nop 0
	ds_add_rtn_u32 v59, v59, v64 offset:17408
	s_mov_b64 exec, s[12:13]
	v_lshlrev_b32_sdwa v60, v63, v8 dst_sel:DWORD dst_unused:UNUSED_PAD src0_sel:DWORD src1_sel:BYTE_0
	s_nop 0
	ds_add_rtn_u32 v60, v60, v64 offset:17408
	s_mov_b64 exec, s[10:11]
	v_lshlrev_b32_sdwa v61, v63, v9 dst_sel:DWORD dst_unused:UNUSED_PAD src0_sel:DWORD src1_sel:BYTE_0
	s_nop 0
	ds_add_rtn_u32 v61, v61, v64 offset:17408
	s_waitcnt lgkmcnt(0)
	s_mov_b64 exec, s[16:17]
	v_lshlrev_b32_e32 v58, 1, v58
	v_lshrrev_b32_e32 v62, 8, v6
	ds_write_b16 v58, v62
	s_mov_b64 exec, s[14:15]
	v_lshlrev_b32_e32 v59, 1, v59
	v_lshrrev_b32_e32 v62, 8, v7
	ds_write_b16 v59, v62
	s_mov_b64 exec, s[12:13]
	v_lshlrev_b32_e32 v60, 1, v60
	v_lshrrev_b32_e32 v62, 8, v8
	ds_write_b16 v60, v62
	s_mov_b64 exec, s[10:11]
	v_lshlrev_b32_e32 v61, 1, v61
	v_lshrrev_b32_e32 v62, 8, v9
	ds_write_b16 v61, v62
	s_cmp_eq_u64 s[8:9], 0
	s_cbranch_scc1 .Lcsr_fast_done
	s_mov_b64 exec, s[8:9]
	v_lshlrev_b32_sdwa v58, v63, v2 dst_sel:DWORD dst_unused:UNUSED_PAD src0_sel:DWORD src1_sel:BYTE_0
	s_nop 0
	ds_add_rtn_u32 v58, v58, v64 offset:17408
	s_mov_b64 exec, s[6:7]
	v_lshlrev_b32_sdwa v59, v63, v3 dst_sel:DWORD dst_unused:UNUSED_PAD src0_sel:DWORD src1_sel:BYTE_0
	s_nop 0
	ds_add_rtn_u32 v59, v59, v64 offset:17408
	s_mov_b64 exec, s[4:5]
	v_lshlrev_b32_sdwa v60, v63, v4 dst_sel:DWORD dst_unused:UNUSED_PAD src0_sel:DWORD src1_sel:BYTE_0
	s_nop 0
	ds_add_rtn_u32 v60, v60, v64 offset:17408
	s_mov_b64 exec, s[68:69]
	v_lshlrev_b32_sdwa v61, v63, v5 dst_sel:DWORD dst_unused:UNUSED_PAD src0_sel:DWORD src1_sel:BYTE_0
	s_nop 0
	ds_add_rtn_u32 v61, v61, v64 offset:17408
	s_waitcnt lgkmcnt(0)
	s_mov_b64 exec, s[8:9]
	v_lshlrev_b32_e32 v58, 1, v58
	v_lshrrev_b32_e32 v62, 8, v2
	ds_write_b16 v58, v62
	s_mov_b64 exec, s[6:7]
	v_lshlrev_b32_e32 v59, 1, v59
	v_lshrrev_b32_e32 v62, 8, v3
	ds_write_b16 v59, v62
	s_mov_b64 exec, s[4:5]
	v_lshlrev_b32_e32 v60, 1, v60
	v_lshrrev_b32_e32 v62, 8, v4
	ds_write_b16 v60, v62
	s_mov_b64 exec, s[68:69]
	v_lshlrev_b32_e32 v61, 1, v61
	v_lshrrev_b32_e32 v62, 8, v5
	ds_write_b16 v61, v62
.Lcsr_fast_done:
	s_mov_b64 exec, s[74:75]
	s_branch .Lcsr_after
.Lcsr_slow:
	s_and_saveexec_b64 s[74:75], s[30:31]
	s_cbranch_execz .LBB1_61
	v_mov_b32_e32 v36, 2
	s_waitcnt vmcnt(4)
	v_lshlrev_b32_sdwa v36, v36, v30 dst_sel:DWORD dst_unused:UNUSED_PAD src0_sel:DWORD src1_sel:BYTE_0
	v_mov_b32_e32 v37, 1
	ds_add_rtn_u32 v36, v36, v37 offset:17408
	v_lshrrev_b32_e32 v30, 8, v30
	s_mov_b64 s[30:31], -1
	s_and_b64 vcc, exec, s[72:73]
	s_cbranch_vccz .LBB1_59
	s_waitcnt lgkmcnt(0)
	v_add_u32_e32 v38, s70, v36
	v_ashrrev_i32_e32 v39, 31, v38
	v_lshl_add_u64 v[38:39], v[38:39], 1, s[76:77]
	global_store_short v[38:39], v30, off
	s_mov_b64 s[30:31], 0

.Lcsr_after:
	s_and_saveexec_b64 s[4:5], s[0:1]
	s_cbranch_execz .LBB1_223
	s_waitcnt vmcnt(3) lgkmcnt(0)
	v_lshl_add_u64 v[2:3], s[84:85], 0, v[34:35]
	s_mov_b64 s[0:1], 0x80
	v_lshl_add_u64 v[2:3], v[2:3], 0, s[0:1]
	s_mov_b32 s8, 32
	s_mov_b64 s[0:1], 0
	v_mov_b32_e32 v4, 1
	v_mov_b32_e32 v5, 2
	s_branch .LBB1_219

	.amdhsa_kernel _Z5k_csrPKiPKjP15HIP_vector_typeIiLj2EEPfPtS6_
		.amdhsa_group_segment_fixed_size 18452
		.amdhsa_private_segment_fixed_size 0
		.amdhsa_kernarg_size 48
		.amdhsa_user_sgpr_count 2
		.amdhsa_user_sgpr_dispatch_ptr 0
		.amdhsa_user_sgpr_queue_ptr 0
		.amdhsa_user_sgpr_kernarg_segment_ptr 1
		.amdhsa_user_sgpr_dispatch_id 0
		.amdhsa_user_sgpr_kernarg_preload_length 0
		.amdhsa_user_sgpr_kernarg_preload_offset 0
		.amdhsa_user_sgpr_private_segment_size 0
		.amdhsa_uses_dynamic_stack 0
		.amdhsa_enable_private_segment 0
		.amdhsa_system_sgpr_workgroup_id_x 1
		.amdhsa_system_sgpr_workgroup_id_y 0
		.amdhsa_system_sgpr_workgroup_id_z 0
		.amdhsa_system_sgpr_workgroup_info 0
		.amdhsa_system_vgpr_workitem_id 0
		.amdhsa_next_free_vgpr 65
		.amdhsa_next_free_sgpr 88
		.amdhsa_accum_offset 68
		.amdhsa_reserve_vcc 1
		.amdhsa_float_round_mode_32 0
		.amdhsa_float_round_mode_16_64 0
		.amdhsa_float_denorm_mode_32 3
		.amdhsa_float_denorm_mode_16_64 3
		.amdhsa_dx10_clamp 1
		.amdhsa_ieee_mode 1
		.amdhsa_fp16_overflow 0
		.amdhsa_tg_split 0
		.amdhsa_exception_fp_ieee_invalid_op 0
		.amdhsa_exception_fp_denorm_src 0
		.amdhsa_exception_fp_ieee_div_zero 0
		.amdhsa_exception_fp_ieee_overflow 0
		.amdhsa_exception_fp_ieee_underflow 0
		.amdhsa_exception_fp_ieee_inexact 0
		.amdhsa_exception_int_div_zero 0
	.end_amdhsa_kernel

amdhsa.kernels:
  - .agpr_count:     0
    .args:
      - .actual_access:  read_only
        .address_space:  global
        .offset:         0
        .size:           8
        .value_kind:     global_buffer
      - .actual_access:  write_only
        .address_space:  global
        .offset:         8
        .size:           8
        .value_kind:     global_buffer
      - .actual_access:  write_only
        .address_space:  global
        .offset:         16
        .size:           8
        .value_kind:     global_buffer
      - .actual_access:  read_only
        .address_space:  global
        .offset:         24
        .size:           8
        .value_kind:     global_buffer
      - .actual_access:  write_only
        .address_space:  global
        .offset:         32
        .size:           8
        .value_kind:     global_buffer
      - .actual_access:  write_only
        .address_space:  global
        .offset:         40
        .size:           8
        .value_kind:     global_buffer
    .group_segment_fixed_size: 14576
    .kernarg_segment_align: 8
    .kernarg_segment_size: 48
    .language:       OpenCL C
    .language_version:
      - 2
      - 0
    .max_flat_workgroup_size: 256
    .name:           _Z5k_binPKiPiPjPKfPDv8_DF16_PDF16_
    .private_segment_fixed_size: 0
    .sgpr_count:     22
    .sgpr_spill_count: 0
    .symbol:         _Z5k_binPKiPiPjPKfPDv8_DF16_PDF16_.kd
    .uniform_work_group_size: 1
    .uses_dynamic_stack: false
    .vgpr_count:     62
    .vgpr_spill_count: 0
    .wavefront_size: 64
  - .agpr_count:     0
    .args:
      - .actual_access:  read_only
        .address_space:  global
        .offset:         0
        .size:           8
        .value_kind:     global_buffer
      - .actual_access:  read_only
        .address_space:  global
        .offset:         8
        .size:           8
        .value_kind:     global_buffer
      - .actual_access:  write_only
        .address_space:  global
        .offset:         16
        .size:           8
        .value_kind:     global_buffer
      - .actual_access:  write_only
        .address_space:  global
        .offset:         24
        .size:           8
        .value_kind:     global_buffer
      - .actual_access:  write_only
        .address_space:  global
        .offset:         32
        .size:           8
        .value_kind:     global_buffer
      - .actual_access:  write_only
        .address_space:  global
        .offset:         40
        .size:           8
        .value_kind:     global_buffer
    .group_segment_fixed_size: 18452
    .kernarg_segment_align: 8
    .kernarg_segment_size: 48
    .language:       OpenCL C
    .language_version:
      - 2
      - 0
    .max_flat_workgroup_size: 256
    .name:           _Z5k_csrPKiPKjP15HIP_vector_typeIiLj2EEPfPtS6_
    .private_segment_fixed_size: 0
    .sgpr_count:     94
    .sgpr_spill_count: 0
    .symbol:         _Z5k_csrPKiPKjP15HIP_vector_typeIiLj2EEPfPtS6_.kd
    .uniform_work_group_size: 1
    .uses_dynamic_stack: false
    .vgpr_count:     65
    .vgpr_spill_count: 0
    .wavefront_size: 64
  - .agpr_count:     0
    .args:
      - .actual_access:  read_only
        .address_space:  global
        .offset:         0
        .size:           8
        .value_kind:     global_buffer
      - .actual_access:  read_only
        .address_space:  global
        .offset:         8
        .size:           8
        .value_kind:     global_buffer
      - .actual_access:  read_only
        .address_space:  global
        .offset:         16
        .size:           8
        .value_kind:     global_buffer
      - .actual_access:  read_only
        .address_space:  global
        .offset:         24
        .size:           8
        .value_kind:     global_buffer
      - .actual_access:  write_only
        .address_space:  global
        .offset:         32
        .size:           8
        .value_kind:     global_buffer
    .group_segment_fixed_size: 129152
    .kernarg_segment_align: 8
    .kernarg_segment_size: 40
    .language:       OpenCL C
    .language_version:
      - 2
      - 0
    .max_flat_workgroup_size: 512
    .name:           _Z6k_gemmPKfPKDv8_DF16_S0_S0_PDF16_
    .private_segment_fixed_size: 0
    .sgpr_count:     22
    .sgpr_spill_count: 0
    .symbol:         _Z6k_gemmPKfPKDv8_DF16_S0_S0_PDF16_.kd
    .uniform_work_group_size: 1
    .uses_dynamic_stack: false
    .vgpr_count:     250
    .vgpr_spill_count: 0
    .wavefront_size: 64
  - .agpr_count:     0
    .args:
      - .actual_access:  read_only
        .address_space:  global
        .offset:         0
        .size:           8
        .value_kind:     global_buffer
      - .actual_access:  read_only
        .address_space:  global
        .offset:         8
        .size:           8
        .value_kind:     global_buffer
      - .actual_access:  read_only
        .address_space:  global
        .offset:         16
        .size:           8
        .value_kind:     global_buffer
      - .actual_access:  read_only
        .address_space:  global
        .offset:         24
        .size:           8
        .value_kind:     global_buffer
      - .actual_access:  read_only
        .address_space:  global
        .offset:         32
        .size:           8
        .value_kind:     global_buffer
      - .actual_access:  read_only
        .address_space:  global
        .offset:         40
        .size:           8
        .value_kind:     global_buffer
      - .address_space:  global
        .offset:         48
        .size:           8
        .value_kind:     global_buffer
    .group_segment_fixed_size: 2304
    .kernarg_segment_align: 8
    .kernarg_segment_size: 56
    .language:       OpenCL C
    .language_version:
      - 2
      - 0
    .max_flat_workgroup_size: 320
    .name:           _Z6k_agg1PKDF16_PK15HIP_vector_typeIiLj2EEPKtPKfS8_S8_Pf
    .private_segment_fixed_size: 0
    .sgpr_count:     40
    .sgpr_spill_count: 0
    .symbol:         _Z6k_agg1PKDF16_PK15HIP_vector_typeIiLj2EEPKtPKfS8_S8_Pf.kd
    .uniform_work_group_size: 1
    .uses_dynamic_stack: false
    .vgpr_count:     62
    .vgpr_spill_count: 0
    .wavefront_size: 64
  - .agpr_count:     0
    .args:
      - .actual_access:  read_only
        .address_space:  global
        .offset:         0
        .size:           8
        .value_kind:     global_buffer
      - .actual_access:  read_only
        .address_space:  global
        .offset:         8
        .size:           8
        .value_kind:     global_buffer
      - .actual_access:  read_only
        .address_space:  global
        .offset:         16
        .size:           8
        .value_kind:     global_buffer
      - .actual_access:  read_only
        .address_space:  global
        .offset:         24
        .size:           8
        .value_kind:     global_buffer
      - .actual_access:  read_only
        .address_space:  global
        .offset:         32
        .size:           8
        .value_kind:     global_buffer
      - .actual_access:  write_only
        .address_space:  global
        .offset:         40
        .size:           8
        .value_kind:     global_buffer
    .group_segment_fixed_size: 0
    .kernarg_segment_align: 8
    .kernarg_segment_size: 48
    .language:       OpenCL C
    .language_version:
      - 2
      - 0
    .max_flat_workgroup_size: 256
    .name:           _Z5k_outPKfPK15HIP_vector_typeIiLj2EEPKtS0_S0_Pf
    .private_segment_fixed_size: 0
    .sgpr_count:     18
    .sgpr_spill_count: 0
    .symbol:         _Z5k_outPKfPK15HIP_vector_typeIiLj2EEPKtS0_S0_Pf.kd
    .uniform_work_group_size: 1
    .uses_dynamic_stack: false
    .vgpr_count:     27
    .vgpr_spill_count: 0
    .wavefront_size: 64
